# s5
# baseline (speedup 1.0000x reference)
.LBB1_12:
	s_and_b32 s12, s19, 1
	s_lshr_b32 s13, s19, 1
	s_add_i32 s16, s19, 1
	v_lshl_add_u32 v231, s13, 3, v221
	s_cmp_lg_u32 s19, 3
	s_cselect_b32 s17, s16, 3
	s_waitcnt lgkmcnt(2)
	v_lshlrev_b32_e32 v2, 7, v231
	s_lshl_b32 s14, s12, 6
	v_or3_b32 v160, v2, s14, v220
	s_waitcnt lgkmcnt(0)
	v_mov_b32_e32 v1, v220
	v_lshl_add_u64 v[2:3], v[160:161], 2, s[6:7]
	global_load_dword v232, v[2:3], off
	s_lshl_b32 s14, s17, 2
	s_and_b32 s14, s14, 24
	s_lshl_b32 s13, s13, 9
	v_lshrrev_b32_e32 v3, 5, v1
	s_cmp_eq_u32 s12, 0
	v_add_u32_e32 v2, s14, v221
	v_lshlrev_b32_e32 v206, 4, v3
	s_cselect_b64 s[14:15], -1, 0
	s_cmp_eq_u32 s12, 1
	v_add3_u32 v149, v228, s13, v206
	s_cselect_b64 s[12:13], -1, 0
	s_lshl_b32 s17, s17, 6
	s_and_b32 s17, s17, 64
	v_lshl_or_b32 v2, v2, 7, s17
	v_lshl_add_u32 v234, v1, 4, 0
	v_and_or_b32 v1, v1, 31, v2
	v_mul_lo_u32 v2, v1, 27
	v_add_u32_e32 v233, 0xc000, v234
	v_mad_u64_u32 v[204:205], s[20:21], v3, 14, v[2:3]
	v_add_u32_e32 v202, 13, v2
	s_waitcnt vmcnt(3)
	v_mul_f32_e32 v1, 0.15915494, v222
	v_cos_f32_e32 v2, v1
	v_sin_f32_e32 v1, v1
	v_add_f32_e32 v2, v2, v2
	v_cndmask_b32_e64 v3, v2, v1, s[0:1]
	v_mul_f32_e32 v1, v1, v2
	v_fma_f32 v2, v2, v2, -2.0
	v_cndmask_b32_e64 v4, v2, v1, s[0:1]
	v_mul_f32_e32 v207, v1, v2
	v_fma_f32 v208, v2, v2, -2.0
	v_mul_f32_e32 v2, 0.15915494, v182
	v_cvt_pk_fp8_f32 v131, v225, v3
	v_cos_f32_e32 v3, v2
	v_sin_f32_e32 v2, v2
	v_cndmask_b32_e64 v1, v208, v207, s[0:1]
	v_cvt_pk_fp8_f32 v131, v4, v1 op_sel:[0,0,1]
	v_add_f32_e32 v1, v3, v3
	v_cvt_pk_f16_f32 v1, v2, v1
	v_cvt_pk_fp8_f32 v128, v182, v183
	v_cvt_scalef32_pk_fp8_f16 v132, v1, 1.0
	v_pk_fma_f16 v1, v1, v1, -2.0 op_sel:[1,0,1] op_sel_hi:[1,1,0]
	v_mul_f32_e32 v0, 0.15915494, v183
	v_cvt_scalef32_pk_fp8_f16 v132, v1, 1.0 op_sel:[0,0,1]
	v_pk_fma_f16 v1, v1, v1, -2.0 op_sel:[0,1,1] op_sel_hi:[1,1,0]
	v_cos_f32_e32 v2, v0
	v_cvt_scalef32_pk_fp8_f16 v133, v1, 1.0
	v_pk_fma_f16 v1, v1, v1, -2.0 op_sel:[0,1,1] op_sel_hi:[1,1,0]
	v_sin_f32_e32 v0, v0
	v_cvt_scalef32_pk_fp8_f16 v133, v1, 1.0 op_sel:[0,0,1]
	v_pk_fma_f16 v1, v1, v1, -2.0 op_sel:[0,1,1] op_sel_hi:[1,1,0]
	s_nop 0
	v_cvt_scalef32_pk_fp8_f16 v134, v1, 1.0
	v_pk_fma_f16 v1, v1, v1, -2.0 op_sel:[0,1,1] op_sel_hi:[1,1,0]
	s_nop 0
	v_cvt_scalef32_pk_fp8_f16 v134, v1, 1.0 op_sel:[0,0,1]
	v_add_f32_e32 v1, v2, v2
	v_cvt_pk_f16_f32 v0, v0, v1
	v_cvt_scalef32_pk_fp8_f16 v135, v0, 1.0
	v_pk_fma_f16 v24, v0, v0, -2.0 op_sel:[1,0,1] op_sel_hi:[1,1,0]
	s_waitcnt vmcnt(2)
	v_mul_f32_e32 v0, 0.15915494, v224
	v_cos_f32_e32 v1, v0
	v_sin_f32_e32 v0, v0
	v_add_f32_e32 v1, v1, v1
	v_cndmask_b32_e64 v2, v1, v0, s[0:1]
	v_mul_f32_e32 v0, v0, v1
	v_fma_f32 v1, v1, v1, -2.0
	v_cndmask_b32_e64 v3, v1, v0, s[0:1]
	v_mul_f32_e32 v209, v0, v1
	v_fma_f32 v210, v1, v1, -2.0
	v_mul_f32_e32 v1, 0.15915494, v190
	s_waitcnt vmcnt(1)
	v_cvt_pk_fp8_f32 v19, v223, v2
	v_cos_f32_e32 v2, v1
	v_sin_f32_e32 v1, v1
	v_cndmask_b32_e64 v0, v210, v209, s[0:1]
	v_cvt_pk_fp8_f32 v19, v3, v0 op_sel:[0,0,1]
	v_add_f32_e32 v0, v2, v2
	v_cvt_pk_f16_f32 v0, v1, v0
	v_cvt_scalef32_pk_fp8_f16 v20, v0, 1.0
	v_pk_fma_f16 v0, v0, v0, -2.0 op_sel:[1,0,1] op_sel_hi:[1,1,0]
	v_mul_f32_e32 v1, 0.15915494, v191
	v_cvt_scalef32_pk_fp8_f16 v135, v24, 1.0 op_sel:[0,0,1]
	v_cvt_scalef32_pk_fp8_f16 v20, v0, 1.0 op_sel:[0,0,1]
	v_pk_fma_f16 v0, v0, v0, -2.0 op_sel:[0,1,1] op_sel_hi:[1,1,0]
	v_cos_f32_e32 v2, v1
	v_pk_fma_f16 v24, v24, v24, -2.0 op_sel:[0,1,1] op_sel_hi:[1,1,0]
	v_cvt_scalef32_pk_fp8_f16 v21, v0, 1.0
	v_pk_fma_f16 v0, v0, v0, -2.0 op_sel:[0,1,1] op_sel_hi:[1,1,0]
	v_sin_f32_e32 v1, v1
	v_pk_fma_f16 v35, v24, v24, -2.0 op_sel:[0,1,1] op_sel_hi:[1,1,0]
	v_cvt_pk_fp8_f32 v128, v184, v185 op_sel:[0,0,1]
	v_cvt_scalef32_pk_fp8_f16 v21, v0, 1.0 op_sel:[0,0,1]
	v_pk_fma_f16 v0, v0, v0, -2.0 op_sel:[0,1,1] op_sel_hi:[1,1,0]
	v_pk_fma_f16 v36, v35, v35, -2.0 op_sel:[0,1,1] op_sel_hi:[1,1,0]
	v_mul_f32_e32 v25, 0.15915494, v184
	v_cvt_pk_fp8_f32 v129, v198, v199
	v_cvt_pk_fp8_f32 v130, v178, v200
	v_cvt_pk_fp8_f32 v16, v190, v191
	v_cvt_pk_fp8_f32 v17, v194, v195
	v_cvt_pk_fp8_f32 v18, v186, v187
	v_cvt_scalef32_pk_fp8_f16 v22, v0, 1.0
	v_pk_fma_f16 v0, v0, v0, -2.0 op_sel:[0,1,1] op_sel_hi:[1,1,0]
	v_pk_fma_f16 v37, v36, v36, -2.0 op_sel:[0,1,1] op_sel_hi:[1,1,0]
	v_cvt_scalef32_pk_fp8_f16 v137, v36, 1.0
	v_cos_f32_e32 v36, v25
	v_cvt_scalef32_pk_fp8_f16 v22, v0, 1.0 op_sel:[0,0,1]
	v_add_f32_e32 v0, v2, v2
	v_sin_f32_e32 v25, v25
	v_cvt_pk_f16_f32 v0, v1, v0
	v_mov_b32_e32 v160, v204
	v_cvt_scalef32_pk_fp8_f16 v23, v0, 1.0
	v_pk_fma_f16 v34, v0, v0, -2.0 op_sel:[1,0,1] op_sel_hi:[1,1,0]
	ds_read_b128 v[26:29], v234
	ds_read_b128 v[30:33], v234 offset:1024
	ds_read_b128 v[8:11], v234 offset:2048
	ds_read_b128 v[12:15], v234 offset:3072
	ds_read_b128 v[0:3], v234 offset:4096
	ds_read_b128 v[4:7], v234 offset:5120
	ds_read_b128 v[152:155], v234 offset:6144
	ds_read_b128 v[156:159], v234 offset:7168
	ds_read_b128 v[96:99], v149
	ds_read_b128 v[100:103], v149 offset:32
	ds_read_b128 v[104:107], v149 offset:64
	ds_read_b128 v[108:111], v149 offset:96
	v_cvt_pk_fp8_f32 v129, v163, v201 op_sel:[0,0,1]
	v_cvt_pk_fp8_f32 v130, v179, v181 op_sel:[0,0,1]
	v_cvt_pk_fp8_f32 v16, v192, v193 op_sel:[0,0,1]
	v_cvt_pk_fp8_f32 v17, v196, v197 op_sel:[0,0,1]
	v_cvt_pk_fp8_f32 v18, v188, v189 op_sel:[0,0,1]
	v_cvt_scalef32_pk_fp8_f16 v136, v24, 1.0
	v_add_f32_e32 v24, v36, v36
	v_cvt_pk_f16_f32 v24, v25, v24
	v_pk_fma_f16 v25, v24, v24, -2.0 op_sel:[1,0,1] op_sel_hi:[1,1,0]
	v_cvt_scalef32_pk_fp8_f16 v138, v24, 1.0
	v_cvt_scalef32_pk_fp8_f16 v23, v34, 1.0 op_sel:[0,0,1]
	v_cvt_scalef32_pk_fp8_f16 v136, v35, 1.0 op_sel:[0,0,1]
	v_pk_fma_f16 v35, v25, v25, -2.0 op_sel:[0,1,1] op_sel_hi:[1,1,0]
	v_cvt_scalef32_pk_fp8_f16 v138, v25, 1.0 op_sel:[0,0,1]
	v_mul_f32_e32 v25, 0.15915494, v185
	s_waitcnt lgkmcnt(0)
	v_mfma_scale_f32_32x32x64_f8f6f4 v[112:127], v[26:33], v[16:23], v[96:111], v227, v226 op_sel_hi:[0,0,0]
	v_cvt_scalef32_pk_fp8_f16 v139, v35, 1.0
	v_pk_fma_f16 v35, v35, v35, -2.0 op_sel:[0,1,1] op_sel_hi:[1,1,0]
	s_nop 0
	v_pk_fma_f16 v24, v35, v35, -2.0 op_sel:[0,1,1] op_sel_hi:[1,1,0]
	ds_read_b128 v[64:67], v149 offset:128
	ds_read_b128 v[68:71], v149 offset:160
	ds_read_b128 v[72:75], v149 offset:192
	ds_read_b128 v[76:79], v149 offset:224
	v_cvt_scalef32_pk_fp8_f16 v140, v24, 1.0
	v_pk_fma_f16 v24, v24, v24, -2.0 op_sel:[0,1,1] op_sel_hi:[1,1,0]
	v_cvt_scalef32_pk_fp8_f16 v137, v37, 1.0 op_sel:[0,0,1]
	v_cvt_scalef32_pk_fp8_f16 v140, v24, 1.0 op_sel:[0,0,1]
	v_cvt_scalef32_pk_fp8_f16 v139, v35, 1.0 op_sel:[0,0,1]
	v_mfma_scale_f32_32x32x64_f8f6f4 v[96:111], v[26:33], v[128:135], v[96:111], v227, v226 op_sel_hi:[0,0,0]
	v_cos_f32_e32 v26, v25
	v_sin_f32_e32 v25, v25
	v_mul_f32_e32 v30, 0.15915494, v192
	v_mul_f32_e32 v31, 0.15915494, v193
	v_add_f32_e32 v24, v26, v26
	v_cvt_pk_f16_f32 v24, v25, v24
	v_cvt_scalef32_pk_fp8_f16 v141, v24, 1.0
	v_pk_fma_f16 v24, v24, v24, -2.0 op_sel:[1,0,1] op_sel_hi:[1,1,0]
	s_nop 0
	v_cvt_scalef32_pk_fp8_f16 v141, v24, 1.0 op_sel:[0,0,1]
	v_pk_fma_f16 v26, v24, v24, -2.0 op_sel:[0,1,1] op_sel_hi:[1,1,0]
	v_lshl_add_u64 v[24:25], v[160:161], 2, s[4:5]
	v_pk_fma_f16 v27, v26, v26, -2.0 op_sel:[0,1,1] op_sel_hi:[1,1,0]
	s_nop 0
	v_pk_fma_f16 v28, v27, v27, -2.0 op_sel:[0,1,1] op_sel_hi:[1,1,0]
	s_waitcnt lgkmcnt(0)
	v_mfma_scale_f32_32x32x64_f8f6f4 v[80:95], v[8:15], v[16:23], v[64:79], v227, v226 op_sel_hi:[0,0,0]
	global_load_dwordx4 v[182:185], v[24:25], off
	global_load_dwordx4 v[190:193], v[24:25], off offset:3456
	v_cos_f32_e32 v25, v31
	v_pk_fma_f16 v29, v28, v28, -2.0 op_sel:[0,1,1] op_sel_hi:[1,1,0]
	v_cvt_scalef32_pk_fp8_f16 v143, v28, 1.0
	v_cvt_scalef32_pk_fp8_f16 v142, v26, 1.0
	v_cvt_scalef32_pk_fp8_f16 v143, v29, 1.0 op_sel:[0,0,1]
	v_cvt_scalef32_pk_fp8_f16 v142, v27, 1.0 op_sel:[0,0,1]
	v_add_f32_e32 v150, v25, v25
	v_mfma_scale_f32_32x32x64_f8f6f4 v[64:79], v[8:15], v[128:135], v[64:79], v227, v226 op_sel_hi:[0,0,0]
	v_pk_fma_f16 v8, v34, v34, -2.0 op_sel:[0,1,1] op_sel_hi:[1,1,0]
	ds_read_b128 v[32:35], v149 offset:256
	ds_read_b128 v[36:39], v149 offset:288
	ds_read_b128 v[40:43], v149 offset:320
	ds_read_b128 v[44:47], v149 offset:352
	v_pk_fma_f16 v9, v8, v8, -2.0 op_sel:[0,1,1] op_sel_hi:[1,1,0]
	v_cvt_scalef32_pk_fp8_f16 v144, v8, 1.0
	v_pk_fma_f16 v10, v9, v9, -2.0 op_sel:[0,1,1] op_sel_hi:[1,1,0]
	v_cvt_scalef32_pk_fp8_f16 v144, v9, 1.0 op_sel:[0,0,1]
	v_pk_fma_f16 v11, v10, v10, -2.0 op_sel:[0,1,1] op_sel_hi:[1,1,0]
	v_cvt_scalef32_pk_fp8_f16 v145, v10, 1.0
	v_cos_f32_e32 v10, v30
	v_cvt_scalef32_pk_fp8_f16 v145, v11, 1.0 op_sel:[0,0,1]
	v_sin_f32_e32 v11, v30
	v_add_f32_e32 v8, v10, v10
	v_cvt_pk_f16_f32 v8, v11, v8
	v_pk_fma_f16 v9, v8, v8, -2.0 op_sel:[1,0,1] op_sel_hi:[1,1,0]
	v_cvt_scalef32_pk_fp8_f16 v146, v8, 1.0
	v_pk_fma_f16 v10, v9, v9, -2.0 op_sel:[0,1,1] op_sel_hi:[1,1,0]
	s_waitcnt lgkmcnt(0)
	v_mfma_scale_f32_32x32x64_f8f6f4 v[48:63], v[0:7], v[16:23], v[32:47], v227, v226 op_sel_hi:[0,0,0]
	v_cvt_scalef32_pk_fp8_f16 v147, v10, 1.0
	v_pk_fma_f16 v10, v10, v10, -2.0 op_sel:[0,1,1] op_sel_hi:[1,1,0]
	v_cvt_scalef32_pk_fp8_f16 v146, v9, 1.0 op_sel:[0,0,1]
	v_cvt_scalef32_pk_fp8_f16 v147, v10, 1.0 op_sel:[0,0,1]
	v_pk_fma_f16 v24, v10, v10, -2.0 op_sel:[0,1,1] op_sel_hi:[1,1,0]
	s_nop 0
	v_cvt_scalef32_pk_fp8_f16 v148, v24, 1.0
	v_pk_fma_f16 v24, v24, v24, -2.0 op_sel:[0,1,1] op_sel_hi:[1,1,0]
	s_nop 0
	v_cvt_scalef32_pk_fp8_f16 v148, v24, 1.0 op_sel:[0,0,1]
	v_mfma_scale_f32_32x32x64_f8f6f4 v[32:47], v[0:7], v[128:135], v[32:47], v227, v226 op_sel_hi:[0,0,0]
	ds_read_b128 v[0:3], v149 offset:384
	ds_read_b128 v[4:7], v149 offset:416
	ds_read_b128 v[8:11], v149 offset:448
	ds_read_b128 v[12:15], v149 offset:480
	v_sin_f32_e32 v149, v31
	s_nop 0
	v_cvt_pk_f16_f32 v150, v149, v150
	v_cvt_scalef32_pk_fp8_f16 v149, v150, 1.0
	v_pk_fma_f16 v150, v150, v150, -2.0 op_sel:[1,0,1] op_sel_hi:[1,1,0]
	s_nop 0
	v_pk_fma_f16 v160, v150, v150, -2.0 op_sel:[0,1,1] op_sel_hi:[1,1,0]
	v_cvt_scalef32_pk_fp8_f16 v149, v150, 1.0 op_sel:[0,0,1]
	v_pk_fma_f16 v164, v160, v160, -2.0 op_sel:[0,1,1] op_sel_hi:[1,1,0]
	s_nop 0
	v_pk_fma_f16 v150, v164, v164, -2.0 op_sel:[0,1,1] op_sel_hi:[1,1,0]
	s_waitcnt lgkmcnt(0)
	v_mfma_scale_f32_32x32x64_f8f6f4 v[16:31], v[152:159], v[16:23], v[0:15], v227, v226 op_sel_hi:[0,0,0]
	v_pk_fma_f16 v165, v150, v150, -2.0 op_sel:[0,1,1] op_sel_hi:[1,1,0]
	v_cvt_scalef32_pk_fp8_f16 v151, v150, 1.0
	v_cvt_scalef32_pk_fp8_f16 v150, v160, 1.0
	v_cvt_scalef32_pk_fp8_f16 v151, v165, 1.0 op_sel:[0,0,1]
	v_cvt_scalef32_pk_fp8_f16 v150, v164, 1.0 op_sel:[0,0,1]
	v_mfma_scale_f32_32x32x64_f8f6f4 v[0:15], v[152:159], v[128:135], v[0:15], v227, v226 op_sel_hi:[0,0,0]
	v_mul_f32_e32 v128, 0.15915494, v198
	v_cos_f32_e32 v129, v128
	v_sin_f32_e32 v128, v128
	v_mul_f32_e32 v133, 0.15915494, v199
	v_cos_f32_e32 v134, v133
	v_add_f32_e32 v129, v129, v129
	v_cvt_pk_f16_f32 v130, v128, v129
	v_pk_fma_f16 v131, v130, v130, -2.0 op_sel:[1,0,1] op_sel_hi:[1,1,0]
	v_sin_f32_e32 v133, v133
	v_pk_fma_f16 v128, v131, v131, -2.0 op_sel:[0,1,1] op_sel_hi:[1,1,0]
	s_nop 0
	v_pk_fma_f16 v132, v128, v128, -2.0 op_sel:[0,1,1] op_sel_hi:[1,1,0]
	v_cvt_scalef32_pk_fp8_f16 v129, v128, 1.0
	v_cvt_scalef32_pk_fp8_f16 v128, v130, 1.0
	v_add_f32_e32 v130, v134, v134
	v_cvt_scalef32_pk_fp8_f16 v128, v131, 1.0 op_sel:[0,0,1]
	v_cvt_pk_f16_f32 v130, v133, v130
	v_cvt_scalef32_pk_fp8_f16 v129, v132, 1.0 op_sel:[0,0,1]
	v_cvt_scalef32_pk_fp8_f16 v131, v130, 1.0
	v_pk_fma_f16 v133, v130, v130, -2.0 op_sel:[1,0,1] op_sel_hi:[1,1,0]
	v_pk_fma_f16 v132, v132, v132, -2.0 op_sel:[0,1,1] op_sel_hi:[1,1,0]
	ds_read_b128 v[152:155], v234 offset:8192
	ds_read_b128 v[156:159], v234 offset:9216
	ds_read_b128 v[164:167], v234 offset:10240
	ds_read_b128 v[168:171], v234 offset:11264
	ds_read_b128 v[236:239], v234 offset:12288
	ds_read_b128 v[240:243], v234 offset:13312
	v_cvt_scalef32_pk_fp8_f16 v130, v132, 1.0
	v_pk_fma_f16 v132, v132, v132, -2.0 op_sel:[0,1,1] op_sel_hi:[1,1,0]
	v_mul_f32_e32 v135, 0.15915494, v163
	s_waitcnt lgkmcnt(4)
	v_mfma_scale_f32_32x32x64_f8f6f4 v[96:111], v[152:159], v[136:143], v[96:111], v227, v226 op_sel_hi:[0,0,0]
	v_cvt_scalef32_pk_fp8_f16 v131, v133, 1.0 op_sel:[0,0,1]
	v_pk_fma_f16 v133, v133, v133, -2.0 op_sel:[0,1,1] op_sel_hi:[1,1,0]
	v_cvt_scalef32_pk_fp8_f16 v130, v132, 1.0 op_sel:[0,0,1]
	v_cvt_scalef32_pk_fp8_f16 v132, v133, 1.0
	v_pk_fma_f16 v133, v133, v133, -2.0 op_sel:[0,1,1] op_sel_hi:[1,1,0]
	ds_read_b128 v[244:247], v234 offset:14336
	ds_read_b128 v[248:251], v234 offset:15360
	v_pk_fma_f16 v134, v133, v133, -2.0 op_sel:[0,1,1] op_sel_hi:[1,1,0]
	v_cvt_scalef32_pk_fp8_f16 v132, v133, 1.0 op_sel:[0,0,1]
	v_cvt_scalef32_pk_fp8_f16 v133, v134, 1.0
	v_pk_fma_f16 v134, v134, v134, -2.0 op_sel:[0,1,1] op_sel_hi:[1,1,0]
	s_nop 0
	v_cvt_scalef32_pk_fp8_f16 v133, v134, 1.0 op_sel:[0,0,1]
	v_mfma_scale_f32_32x32x64_f8f6f4 v[112:127], v[152:159], v[144:151], v[112:127], v227, v226 op_sel_hi:[0,0,0]
	v_cos_f32_e32 v152, v135
	v_sin_f32_e32 v135, v135
	v_mul_f32_e32 v154, 0.15915494, v194
	v_cos_f32_e32 v155, v154
	v_add_f32_e32 v134, v152, v152
	v_cvt_pk_f16_f32 v152, v135, v134
	v_pk_fma_f16 v153, v152, v152, -2.0 op_sel:[1,0,1] op_sel_hi:[1,1,0]
	v_sin_f32_e32 v154, v154
	v_pk_fma_f16 v134, v153, v153, -2.0 op_sel:[0,1,1] op_sel_hi:[1,1,0]
	s_nop 0
	v_pk_fma_f16 v160, v134, v134, -2.0 op_sel:[0,1,1] op_sel_hi:[1,1,0]
	v_cvt_scalef32_pk_fp8_f16 v135, v134, 1.0
	v_cvt_scalef32_pk_fp8_f16 v134, v152, 1.0
	v_add_f32_e32 v152, v155, v155
	s_waitcnt lgkmcnt(4)
	v_mfma_scale_f32_32x32x64_f8f6f4 v[64:79], v[164:171], v[136:143], v[64:79], v227, v226 op_sel_hi:[0,0,0]
	v_mul_f32_e32 v157, 0.15915494, v195
	v_cvt_pk_f16_f32 v154, v154, v152
	v_cos_f32_e32 v158, v157
	v_pk_fma_f16 v155, v154, v154, -2.0 op_sel:[1,0,1] op_sel_hi:[1,1,0]
	v_sin_f32_e32 v157, v157
	v_pk_fma_f16 v152, v155, v155, -2.0 op_sel:[0,1,1] op_sel_hi:[1,1,0]
	v_cvt_scalef32_pk_fp8_f16 v134, v153, 1.0 op_sel:[0,0,1]
	v_pk_fma_f16 v156, v152, v152, -2.0 op_sel:[0,1,1] op_sel_hi:[1,1,0]
	v_cvt_scalef32_pk_fp8_f16 v153, v152, 1.0
	v_cvt_scalef32_pk_fp8_f16 v152, v154, 1.0
	v_add_f32_e32 v154, v158, v158
	v_mul_f32_e32 v159, 0.15915494, v196
	v_cvt_scalef32_pk_fp8_f16 v152, v155, 1.0 op_sel:[0,0,1]
	v_mfma_scale_f32_32x32x64_f8f6f4 v[80:95], v[164:171], v[144:151], v[80:95], v227, v226 op_sel_hi:[0,0,0]
	v_cvt_pk_f16_f32 v154, v157, v154
	v_cvt_scalef32_pk_fp8_f16 v153, v156, 1.0 op_sel:[0,0,1]
	v_cvt_scalef32_pk_fp8_f16 v155, v154, 1.0
	v_pk_fma_f16 v156, v156, v156, -2.0 op_sel:[0,1,1] op_sel_hi:[1,1,0]
	v_pk_fma_f16 v157, v154, v154, -2.0 op_sel:[1,0,1] op_sel_hi:[1,1,0]
	v_cvt_scalef32_pk_fp8_f16 v154, v156, 1.0
	v_pk_fma_f16 v156, v156, v156, -2.0 op_sel:[0,1,1] op_sel_hi:[1,1,0]
	v_cvt_scalef32_pk_fp8_f16 v155, v157, 1.0 op_sel:[0,0,1]
	v_pk_fma_f16 v157, v157, v157, -2.0 op_sel:[0,1,1] op_sel_hi:[1,1,0]
	v_cvt_scalef32_pk_fp8_f16 v154, v156, 1.0 op_sel:[0,0,1]
	v_cvt_scalef32_pk_fp8_f16 v156, v157, 1.0
	v_pk_fma_f16 v157, v157, v157, -2.0 op_sel:[0,1,1] op_sel_hi:[1,1,0]
	s_waitcnt lgkmcnt(0)
	v_mfma_scale_f32_32x32x64_f8f6f4 v[0:15], v[244:251], v[136:143], v[0:15], v227, v226 op_sel_hi:[0,0,0]
	v_cvt_scalef32_pk_fp8_f16 v156, v157, 1.0 op_sel:[0,0,1]
	v_pk_fma_f16 v158, v157, v157, -2.0 op_sel:[0,1,1] op_sel_hi:[1,1,0]
	v_cvt_scalef32_pk_fp8_f16 v135, v160, 1.0 op_sel:[0,0,1]
	v_cvt_scalef32_pk_fp8_f16 v157, v158, 1.0
	v_mfma_scale_f32_32x32x64_f8f6f4 v[32:47], v[236:243], v[136:143], v[32:47], v227, v226 op_sel_hi:[0,0,0]
	v_cos_f32_e32 v136, v159
	v_sin_f32_e32 v137, v159
	v_pk_fma_f16 v138, v158, v158, -2.0 op_sel:[0,1,1] op_sel_hi:[1,1,0]
	v_add_f32_e32 v136, v136, v136
	v_cvt_pk_f16_f32 v136, v137, v136
	v_pk_fma_f16 v137, v136, v136, -2.0 op_sel:[1,0,1] op_sel_hi:[1,1,0]
	v_cvt_scalef32_pk_fp8_f16 v157, v138, 1.0 op_sel:[0,0,1]
	v_pk_fma_f16 v138, v137, v137, -2.0 op_sel:[0,1,1] op_sel_hi:[1,1,0]
	s_nop 0
	v_pk_fma_f16 v180, v138, v138, -2.0 op_sel:[0,1,1] op_sel_hi:[1,1,0]
	v_cvt_scalef32_pk_fp8_f16 v159, v138, 1.0
	v_cvt_scalef32_pk_fp8_f16 v158, v136, 1.0
	v_cvt_scalef32_pk_fp8_f16 v159, v180, 1.0 op_sel:[0,0,1]
	v_cvt_scalef32_pk_fp8_f16 v158, v137, 1.0 op_sel:[0,0,1]
	v_mfma_scale_f32_32x32x64_f8f6f4 v[48:63], v[236:243], v[144:151], v[48:63], v227, v226 op_sel_hi:[0,0,0]
	v_mfma_scale_f32_32x32x64_f8f6f4 v[16:31], v[244:251], v[144:151], v[16:31], v227, v226 op_sel_hi:[0,0,0]
	ds_read_b128 v[140:143], v234 offset:16384
	ds_read_b128 v[144:147], v234 offset:17408
	ds_read_b128 v[236:239], v234 offset:18432
	ds_read_b128 v[240:243], v234 offset:19456
	ds_read_b128 v[170:173], v234 offset:20480
	ds_read_b128 v[174:177], v234 offset:21504
	s_waitcnt lgkmcnt(4)
	v_mfma_scale_f32_32x32x64_f8f6f4 v[96:111], v[140:147], v[128:135], v[96:111], v227, v226 op_sel_hi:[0,0,0]
	v_pk_fma_f16 v139, v160, v160, -2.0 op_sel:[0,1,1] op_sel_hi:[1,1,0]
	v_mov_b32_e32 v160, v204
	ds_read_b128 v[162:165], v234 offset:22528
	ds_read_b128 v[166:169], v234 offset:23552
	v_mul_f32_e32 v136, 0.15915494, v201
	v_cos_f32_e32 v137, v136
	v_sin_f32_e32 v136, v136
	v_mul_f32_e32 v150, 0.15915494, v186
	v_cos_f32_e32 v151, v150
	v_add_f32_e32 v137, v137, v137
	v_cvt_pk_f16_f32 v136, v136, v137
	v_pk_fma_f16 v138, v136, v136, -2.0 op_sel:[1,0,1] op_sel_hi:[1,1,0]
	v_cvt_scalef32_pk_fp8_f16 v137, v136, 1.0
	v_mfma_scale_f32_32x32x64_f8f6f4 v[112:127], v[140:147], v[152:159], v[112:127], v227, v226 op_sel_hi:[0,0,0]
	v_mul_f32_e32 v140, 0.15915494, v178
	v_cos_f32_e32 v141, v140
	v_sin_f32_e32 v140, v140
	v_mul_f32_e32 v143, 0.15915494, v200
	v_cos_f32_e32 v144, v143
	v_add_f32_e32 v141, v141, v141
	v_cvt_pk_f16_f32 v141, v140, v141
	v_sin_f32_e32 v143, v143
	v_cvt_scalef32_pk_fp8_f16 v140, v141, 1.0
	v_pk_fma_f16 v141, v141, v141, -2.0 op_sel:[1,0,1] op_sel_hi:[1,1,0]
	v_mul_f32_e32 v146, 0.15915494, v197
	v_pk_fma_f16 v142, v141, v141, -2.0 op_sel:[0,1,1] op_sel_hi:[1,1,0]
	v_cvt_scalef32_pk_fp8_f16 v140, v141, 1.0 op_sel:[0,0,1]
	v_cvt_scalef32_pk_fp8_f16 v141, v142, 1.0
	v_pk_fma_f16 v145, v142, v142, -2.0 op_sel:[0,1,1] op_sel_hi:[1,1,0]
	v_add_f32_e32 v142, v144, v144
	v_cvt_pk_f16_f32 v144, v143, v142
	v_lshl_add_u64 v[142:143], v[160:161], 2, s[4:5]
	global_load_dwordx4 v[198:201], v[142:143], off offset:16
	global_load_dwordx4 v[194:197], v[142:143], off offset:3472
	v_cvt_scalef32_pk_fp8_f16 v141, v145, 1.0 op_sel:[0,0,1]
	v_pk_fma_f16 v160, v144, v144, -2.0 op_sel:[1,0,1] op_sel_hi:[1,1,0]
	v_cvt_scalef32_pk_fp8_f16 v143, v144, 1.0
	v_pk_fma_f16 v144, v145, v145, -2.0 op_sel:[0,1,1] op_sel_hi:[1,1,0]
	v_cos_f32_e32 v145, v146
	v_sin_f32_e32 v146, v146
	v_pk_fma_f16 v148, v138, v138, -2.0 op_sel:[0,1,1] op_sel_hi:[1,1,0]
	v_cvt_scalef32_pk_fp8_f16 v136, v139, 1.0
	v_pk_fma_f16 v139, v139, v139, -2.0 op_sel:[0,1,1] op_sel_hi:[1,1,0]
	v_pk_fma_f16 v149, v148, v148, -2.0 op_sel:[0,1,1] op_sel_hi:[1,1,0]
	v_cvt_scalef32_pk_fp8_f16 v142, v144, 1.0
	v_pk_fma_f16 v144, v144, v144, -2.0 op_sel:[0,1,1] op_sel_hi:[1,1,0]
	v_cvt_scalef32_pk_fp8_f16 v137, v138, 1.0 op_sel:[0,0,1]
	v_cvt_scalef32_pk_fp8_f16 v136, v139, 1.0 op_sel:[0,0,1]
	v_pk_fma_f16 v138, v149, v149, -2.0 op_sel:[0,1,1] op_sel_hi:[1,1,0]
	v_cvt_scalef32_pk_fp8_f16 v142, v144, 1.0 op_sel:[0,0,1]
	v_add_f32_e32 v144, v145, v145
	v_cvt_scalef32_pk_fp8_f16 v139, v138, 1.0
	v_pk_fma_f16 v138, v138, v138, -2.0 op_sel:[0,1,1] op_sel_hi:[1,1,0]
	s_waitcnt lgkmcnt(4)
	v_mfma_scale_f32_32x32x64_f8f6f4 v[64:79], v[236:243], v[128:135], v[64:79], v227, v226 op_sel_hi:[0,0,0]
	v_cvt_pk_f16_f32 v144, v146, v144
	v_cvt_scalef32_pk_fp8_f16 v139, v138, 1.0 op_sel:[0,0,1]
	v_pk_fma_f16 v146, v144, v144, -2.0 op_sel:[1,0,1] op_sel_hi:[1,1,0]
	v_cvt_scalef32_pk_fp8_f16 v138, v148, 1.0
	v_cvt_scalef32_pk_fp8_f16 v145, v144, 1.0
	v_pk_fma_f16 v147, v180, v180, -2.0 op_sel:[0,1,1] op_sel_hi:[1,1,0]
	v_pk_fma_f16 v148, v146, v146, -2.0 op_sel:[0,1,1] op_sel_hi:[1,1,0]
	v_cvt_scalef32_pk_fp8_f16 v138, v149, 1.0 op_sel:[0,0,1]
	v_cvt_scalef32_pk_fp8_f16 v144, v147, 1.0
	v_pk_fma_f16 v147, v147, v147, -2.0 op_sel:[0,1,1] op_sel_hi:[1,1,0]
	v_pk_fma_f16 v149, v148, v148, -2.0 op_sel:[0,1,1] op_sel_hi:[1,1,0]
	v_cvt_scalef32_pk_fp8_f16 v145, v146, 1.0 op_sel:[0,0,1]
	v_mfma_scale_f32_32x32x64_f8f6f4 v[80:95], v[236:243], v[152:159], v[80:95], v227, v226 op_sel_hi:[0,0,0]
	v_pk_fma_f16 v146, v149, v149, -2.0 op_sel:[0,1,1] op_sel_hi:[1,1,0]
	v_cvt_scalef32_pk_fp8_f16 v144, v147, 1.0 op_sel:[0,0,1]
	v_cvt_scalef32_pk_fp8_f16 v147, v146, 1.0
	v_pk_fma_f16 v146, v146, v146, -2.0 op_sel:[0,1,1] op_sel_hi:[1,1,0]
	v_sin_f32_e32 v150, v150
	v_cvt_scalef32_pk_fp8_f16 v147, v146, 1.0 op_sel:[0,0,1]
	v_cvt_scalef32_pk_fp8_f16 v146, v148, 1.0
	v_add_f32_e32 v148, v151, v151
	v_mul_f32_e32 v151, 0.15915494, v187
	v_cvt_scalef32_pk_fp8_f16 v146, v149, 1.0 op_sel:[0,0,1]
	v_cvt_pk_f16_f32 v149, v150, v148
	v_cvt_scalef32_pk_fp8_f16 v148, v149, 1.0
	s_waitcnt lgkmcnt(0)
	v_mfma_scale_f32_32x32x64_f8f6f4 v[0:15], v[162:169], v[128:135], v[0:15], v227, v226 op_sel_hi:[0,0,0]
	v_pk_fma_f16 v149, v149, v149, -2.0 op_sel:[1,0,1] op_sel_hi:[1,1,0]
	v_cvt_scalef32_pk_fp8_f16 v143, v160, 1.0 op_sel:[0,0,1]
	v_pk_fma_f16 v150, v149, v149, -2.0 op_sel:[0,1,1] op_sel_hi:[1,1,0]
	v_cvt_scalef32_pk_fp8_f16 v148, v149, 1.0 op_sel:[0,0,1]
	v_cvt_scalef32_pk_fp8_f16 v149, v150, 1.0
	v_mfma_scale_f32_32x32x64_f8f6f4 v[32:47], v[170:177], v[128:135], v[32:47], v227, v226 op_sel_hi:[0,0,0]
	v_cos_f32_e32 v128, v151
	v_sin_f32_e32 v129, v151
	v_pk_fma_f16 v130, v150, v150, -2.0 op_sel:[0,1,1] op_sel_hi:[1,1,0]
	v_add_f32_e32 v128, v128, v128
	v_cvt_pk_f16_f32 v128, v129, v128
	v_pk_fma_f16 v203, v128, v128, -2.0 op_sel:[1,0,1] op_sel_hi:[1,1,0]
	v_cvt_scalef32_pk_fp8_f16 v151, v128, 1.0
	v_pk_fma_f16 v128, v130, v130, -2.0 op_sel:[0,1,1] op_sel_hi:[1,1,0]
	s_nop 0
	v_cvt_scalef32_pk_fp8_f16 v150, v128, 1.0
	v_pk_fma_f16 v128, v128, v128, -2.0 op_sel:[0,1,1] op_sel_hi:[1,1,0]
	v_cvt_scalef32_pk_fp8_f16 v149, v130, 1.0 op_sel:[0,0,1]
	v_cvt_scalef32_pk_fp8_f16 v151, v203, 1.0 op_sel:[0,0,1]
	v_cvt_scalef32_pk_fp8_f16 v150, v128, 1.0 op_sel:[0,0,1]
	v_mfma_scale_f32_32x32x64_f8f6f4 v[48:63], v[170:177], v[152:159], v[48:63], v227, v226 op_sel_hi:[0,0,0]
	v_mfma_scale_f32_32x32x64_f8f6f4 v[16:31], v[162:169], v[152:159], v[16:31], v227, v226 op_sel_hi:[0,0,0]
	v_pk_fma_f16 v130, v160, v160, -2.0 op_sel:[0,1,1] op_sel_hi:[1,1,0]
	s_nop 0
	v_pk_fma_f16 v131, v130, v130, -2.0 op_sel:[0,1,1] op_sel_hi:[1,1,0]
	ds_read_b128 v[152:155], v234 offset:24576
	ds_read_b128 v[156:159], v234 offset:25600
	ds_read_b128 v[162:165], v234 offset:26624
	ds_read_b128 v[166:169], v234 offset:27648
	v_pk_fma_f16 v128, v131, v131, -2.0 op_sel:[0,1,1] op_sel_hi:[1,1,0]
	v_mov_b32_e32 v160, v204
	v_pk_fma_f16 v132, v128, v128, -2.0 op_sel:[0,1,1] op_sel_hi:[1,1,0]
	v_cvt_scalef32_pk_fp8_f16 v129, v128, 1.0
	v_cvt_scalef32_pk_fp8_f16 v129, v132, 1.0 op_sel:[0,0,1]
	v_mul_f32_e32 v132, 0.15915494, v179
	v_sin_f32_e32 v133, v132
	v_cos_f32_e32 v132, v132
	v_cvt_scalef32_pk_fp8_f16 v128, v130, 1.0
	v_cvt_scalef32_pk_fp8_f16 v128, v131, 1.0 op_sel:[0,0,1]
	v_add_f32_e32 v130, v132, v132
	v_cvt_pk_f16_f32 v132, v133, v130
	v_pk_fma_f16 v133, v132, v132, -2.0 op_sel:[1,0,1] op_sel_hi:[1,1,0]
	s_nop 0
	v_pk_fma_f16 v130, v133, v133, -2.0 op_sel:[0,1,1] op_sel_hi:[1,1,0]
	s_waitcnt lgkmcnt(2)
	v_mfma_scale_f32_32x32x64_f8f6f4 v[96:111], v[152:159], v[136:143], v[96:111], v227, v226 op_sel_hi:[0,0,0]
	v_cvt_scalef32_pk_fp8_f16 v131, v130, 1.0
	v_pk_fma_f16 v134, v130, v130, -2.0 op_sel:[0,1,1] op_sel_hi:[1,1,0]
	v_cvt_scalef32_pk_fp8_f16 v130, v132, 1.0
	v_cvt_scalef32_pk_fp8_f16 v131, v134, 1.0 op_sel:[0,0,1]
	v_cvt_scalef32_pk_fp8_f16 v130, v133, 1.0 op_sel:[0,0,1]
	v_pk_fma_f16 v133, v134, v134, -2.0 op_sel:[0,1,1] op_sel_hi:[1,1,0]
	v_mul_f32_e32 v134, 0.15915494, v181
	v_cos_f32_e32 v135, v134
	v_sin_f32_e32 v134, v134
	v_cvt_scalef32_pk_fp8_f16 v132, v133, 1.0
	v_pk_fma_f16 v133, v133, v133, -2.0 op_sel:[0,1,1] op_sel_hi:[1,1,0]
	ds_read_b128 v[170:173], v234 offset:28672
	ds_read_b128 v[174:177], v234 offset:29696
	ds_read_b128 v[236:239], v234 offset:30720
	ds_read_b128 v[240:243], v234 offset:31744
	v_cvt_scalef32_pk_fp8_f16 v132, v133, 1.0 op_sel:[0,0,1]
	v_add_f32_e32 v133, v135, v135
	v_mfma_scale_f32_32x32x64_f8f6f4 v[112:127], v[152:159], v[144:151], v[112:127], v227, v226 op_sel_hi:[0,0,0]
	v_cvt_pk_f16_f32 v152, v134, v133
	v_mul_f32_e32 v153, 0.15915494, v188
	v_lshl_add_u64 v[134:135], v[160:161], 2, s[4:5]
	v_mul_f32_e32 v154, 0.15915494, v189
	global_load_dwordx4 v[178:181], v[134:135], off offset:32
	global_load_dwordx4 v[186:189], v[134:135], off offset:3488
	v_pk_fma_f16 v134, v152, v152, -2.0 op_sel:[1,0,1] op_sel_hi:[1,1,0]
	v_cvt_scalef32_pk_fp8_f16 v133, v152, 1.0
	v_pk_fma_f16 v152, v134, v134, -2.0 op_sel:[0,1,1] op_sel_hi:[1,1,0]
	v_cvt_scalef32_pk_fp8_f16 v133, v134, 1.0 op_sel:[0,0,1]
	v_pk_fma_f16 v155, v152, v152, -2.0 op_sel:[0,1,1] op_sel_hi:[1,1,0]
	s_nop 0
	v_pk_fma_f16 v134, v155, v155, -2.0 op_sel:[0,1,1] op_sel_hi:[1,1,0]
	s_nop 0
	v_pk_fma_f16 v156, v134, v134, -2.0 op_sel:[0,1,1] op_sel_hi:[1,1,0]
	v_cvt_scalef32_pk_fp8_f16 v135, v134, 1.0
	v_cvt_scalef32_pk_fp8_f16 v134, v152, 1.0
	v_pk_fma_f16 v152, v203, v203, -2.0 op_sel:[0,1,1] op_sel_hi:[1,1,0]
	v_cvt_scalef32_pk_fp8_f16 v134, v155, 1.0 op_sel:[0,0,1]
	v_pk_fma_f16 v155, v152, v152, -2.0 op_sel:[0,1,1] op_sel_hi:[1,1,0]
	s_waitcnt lgkmcnt(4)
	v_mfma_scale_f32_32x32x64_f8f6f4 v[64:79], v[162:169], v[136:143], v[64:79], v227, v226 op_sel_hi:[0,0,0]
	v_cvt_scalef32_pk_fp8_f16 v135, v156, 1.0 op_sel:[0,0,1]
	v_pk_fma_f16 v156, v155, v155, -2.0 op_sel:[0,1,1] op_sel_hi:[1,1,0]
	s_nop 0
	v_pk_fma_f16 v157, v156, v156, -2.0 op_sel:[0,1,1] op_sel_hi:[1,1,0]
	v_mfma_scale_f32_32x32x64_f8f6f4 v[80:95], v[162:169], v[144:151], v[80:95], v227, v226 op_sel_hi:[0,0,0]
	v_cvt_scalef32_pk_fp8_f16 v165, v156, 1.0
	v_cos_f32_e32 v156, v153
	v_sin_f32_e32 v153, v153
	v_cvt_scalef32_pk_fp8_f16 v164, v152, 1.0
	v_add_f32_e32 v152, v156, v156
	v_cvt_pk_f16_f32 v152, v153, v152
	v_pk_fma_f16 v153, v152, v152, -2.0 op_sel:[1,0,1] op_sel_hi:[1,1,0]
	v_cvt_scalef32_pk_fp8_f16 v166, v152, 1.0
	v_cvt_scalef32_pk_fp8_f16 v164, v155, 1.0 op_sel:[0,0,1]
	v_pk_fma_f16 v155, v153, v153, -2.0 op_sel:[0,1,1] op_sel_hi:[1,1,0]
	v_cvt_scalef32_pk_fp8_f16 v166, v153, 1.0 op_sel:[0,0,1]
	s_waitcnt lgkmcnt(0)
	v_mfma_scale_f32_32x32x64_f8f6f4 v[0:15], v[236:243], v[136:143], v[0:15], v227, v226 op_sel_hi:[0,0,0]
	v_cos_f32_e32 v153, v154
	v_cvt_scalef32_pk_fp8_f16 v167, v155, 1.0
	v_pk_fma_f16 v155, v155, v155, -2.0 op_sel:[0,1,1] op_sel_hi:[1,1,0]
	v_sin_f32_e32 v154, v154
	v_pk_fma_f16 v152, v155, v155, -2.0 op_sel:[0,1,1] op_sel_hi:[1,1,0]
	s_nop 0
	v_cvt_scalef32_pk_fp8_f16 v168, v152, 1.0
	v_pk_fma_f16 v152, v152, v152, -2.0 op_sel:[0,1,1] op_sel_hi:[1,1,0]
	s_nop 0
	v_cvt_scalef32_pk_fp8_f16 v168, v152, 1.0 op_sel:[0,0,1]
	v_add_f32_e32 v152, v153, v153
	v_cvt_scalef32_pk_fp8_f16 v165, v157, 1.0 op_sel:[0,0,1]
	v_cvt_scalef32_pk_fp8_f16 v167, v155, 1.0 op_sel:[0,0,1]
	v_mfma_scale_f32_32x32x64_f8f6f4 v[32:47], v[170:177], v[136:143], v[32:47], v227, v226 op_sel_hi:[0,0,0]
	v_cvt_pk_f16_f32 v136, v154, v152
	v_cvt_scalef32_pk_fp8_f16 v169, v136, 1.0
	v_pk_fma_f16 v136, v136, v136, -2.0 op_sel:[1,0,1] op_sel_hi:[1,1,0]
	s_nop 0
	v_cvt_scalef32_pk_fp8_f16 v169, v136, 1.0 op_sel:[0,0,1]
	v_pk_fma_f16 v136, v136, v136, -2.0 op_sel:[0,1,1] op_sel_hi:[1,1,0]
	s_nop 0
	v_pk_fma_f16 v137, v136, v136, -2.0 op_sel:[0,1,1] op_sel_hi:[1,1,0]
	s_nop 0
	v_pk_fma_f16 v138, v137, v137, -2.0 op_sel:[0,1,1] op_sel_hi:[1,1,0]
	s_nop 0
	v_pk_fma_f16 v139, v138, v138, -2.0 op_sel:[0,1,1] op_sel_hi:[1,1,0]
	v_mfma_scale_f32_32x32x64_f8f6f4 v[48:63], v[170:177], v[144:151], v[48:63], v227, v226 op_sel_hi:[0,0,0]
	v_cvt_scalef32_pk_fp8_f16 v171, v138, 1.0
	v_cvt_scalef32_pk_fp8_f16 v170, v136, 1.0
	v_cvt_scalef32_pk_fp8_f16 v171, v139, 1.0 op_sel:[0,0,1]
	v_cvt_scalef32_pk_fp8_f16 v170, v137, 1.0 op_sel:[0,0,1]
	v_mfma_scale_f32_32x32x64_f8f6f4 v[16:31], v[236:243], v[144:151], v[16:31], v227, v226 op_sel_hi:[0,0,0]
	v_mul_f32_e32 v152, 0.15915494, v225
	ds_read_b128 v[136:139], v234 offset:32768
	ds_read_b128 v[140:143], v234 offset:33792
	v_cos_f32_e32 v153, v152
	v_sin_f32_e32 v152, v152
	v_mov_b32_e32 v205, v161
	s_waitcnt lgkmcnt(0)
	v_mfma_scale_f32_32x32x64_f8f6f4 v[96:111], v[136:143], v[128:135], v[96:111], v227, v226 op_sel_hi:[0,0,0]
	v_add_f32_e32 v153, v153, v153
	v_cvt_pk_f16_f32 v158, v152, v153
	v_mov_b32_e32 v203, v161
	v_cndmask_b32_e64 v162, 0, v222, s[0:1]
	v_mul_f32_e32 v163, 0.15915494, v223
	v_pk_fma_f16 v159, v158, v158, -2.0 op_sel:[1,0,1] op_sel_hi:[1,1,0]
	v_cndmask_b32_e64 v172, 0, v224, s[0:1]
	v_pk_fma_f16 v156, v159, v159, -2.0 op_sel:[0,1,1] op_sel_hi:[1,1,0]
	s_nop 0
	v_pk_fma_f16 v160, v156, v156, -2.0 op_sel:[0,1,1] op_sel_hi:[1,1,0]
	v_cvt_scalef32_pk_fp8_f16 v157, v156, 1.0
	v_cvt_scalef32_pk_fp8_f16 v156, v158, 1.0
	v_cvt_scalef32_pk_fp8_f16 v156, v159, 1.0 op_sel:[0,0,1]
	v_mfma_scale_f32_32x32x64_f8f6f4 v[112:127], v[136:143], v[164:171], v[112:127], v227, v226 op_sel_hi:[0,0,0]
	ds_read_b128 v[136:139], v234 offset:34816
	ds_read_b128 v[140:143], v234 offset:35840
	ds_read_b128 v[144:147], v234 offset:36864
	ds_read_b128 v[148:151], v234 offset:37888
	ds_read_b128 v[236:239], v234 offset:38912
	ds_read_b128 v[240:243], v234 offset:39936
	v_lshl_add_u64 v[152:153], v[204:205], 2, s[4:5]
	v_lshl_add_u64 v[154:155], v[202:203], 2, s[4:5]
	global_load_dword v225, v[152:153], off offset:48
	global_load_dword v222, v[154:155], off
	global_load_dword v224, v[154:155], off offset:3456
	global_load_dword v223, v[152:153], off offset:3504
	v_cvt_scalef32_pk_fp8_f16 v157, v160, 1.0 op_sel:[0,0,1]
	s_waitcnt lgkmcnt(4)
	v_mfma_scale_f32_32x32x64_f8f6f4 v[64:79], v[136:143], v[128:135], v[64:79], v227, v226 op_sel_hi:[0,0,0]
	v_mfma_scale_f32_32x32x64_f8f6f4 v[80:95], v[136:143], v[164:171], v[80:95], v227, v226 op_sel_hi:[0,0,0]
	v_mul_f32_e32 v136, v207, v208
	v_fma_f32 v137, v208, v208, -2.0
	v_cndmask_b32_e64 v138, v137, v136, s[0:1]
	v_mul_f32_e32 v136, v136, v137
	v_fma_f32 v137, v137, v137, -2.0
	v_cndmask_b32_e64 v139, v137, v136, s[0:1]
	v_cvt_pk_fp8_f32 v159, v138, v139
	v_mul_f32_e32 v136, v136, v137
	v_fma_f32 v137, v137, v137, -2.0
	v_cndmask_b32_e64 v136, v137, v136, s[0:1]
	v_cvt_pk_fp8_f32 v159, v136, v162 op_sel:[0,0,1]
	v_pk_fma_f16 v136, v160, v160, -2.0 op_sel:[0,1,1] op_sel_hi:[1,1,0]
	v_mov_b32_e32 v160, v161
	v_pk_fma_f16 v137, v136, v136, -2.0 op_sel:[0,1,1] op_sel_hi:[1,1,0]
	v_cvt_scalef32_pk_fp8_f16 v158, v136, 1.0
	v_cos_f32_e32 v136, v163
	v_cvt_scalef32_pk_fp8_f16 v158, v137, 1.0 op_sel:[0,0,1]
	v_sin_f32_e32 v137, v163
	s_waitcnt lgkmcnt(0)
	v_mfma_scale_f32_32x32x64_f8f6f4 v[0:15], v[236:243], v[128:135], v[0:15], v227, v226 op_sel_hi:[0,0,0]
	v_add_f32_e32 v136, v136, v136
	v_mov_b32_e32 v162, v161
	v_cvt_pk_f16_f32 v138, v137, v136
	v_pk_fma_f16 v139, v138, v138, -2.0 op_sel:[1,0,1] op_sel_hi:[1,1,0]
	s_nop 0
	v_pk_fma_f16 v136, v139, v139, -2.0 op_sel:[0,1,1] op_sel_hi:[1,1,0]
	v_mov_b32_e32 v163, v161
	v_pk_fma_f16 v140, v136, v136, -2.0 op_sel:[0,1,1] op_sel_hi:[1,1,0]
	v_cvt_scalef32_pk_fp8_f16 v137, v136, 1.0
	v_cvt_scalef32_pk_fp8_f16 v136, v138, 1.0
	v_cvt_scalef32_pk_fp8_f16 v136, v139, 1.0 op_sel:[0,0,1]
	v_mul_f32_e32 v138, v209, v210
	v_fma_f32 v139, v210, v210, -2.0
	v_cndmask_b32_e64 v141, v139, v138, s[0:1]
	v_mul_f32_e32 v138, v138, v139
	v_fma_f32 v142, v139, v139, -2.0
	v_cndmask_b32_e64 v143, v142, v138, s[0:1]
	v_cvt_pk_fp8_f32 v139, v141, v143
	v_mfma_scale_f32_32x32x64_f8f6f4 v[32:47], v[144:151], v[128:135], v[32:47], v227, v226 op_sel_hi:[0,0,0]
	v_mul_f32_e32 v128, v138, v142
	v_fma_f32 v129, v142, v142, -2.0
	v_cndmask_b32_e64 v128, v129, v128, s[0:1]
	v_cvt_pk_fp8_f32 v139, v128, v172 op_sel:[0,0,1]
	v_pk_fma_f16 v128, v140, v140, -2.0 op_sel:[0,1,1] op_sel_hi:[1,1,0]
	s_nop 0
	v_cvt_scalef32_pk_fp8_f16 v138, v128, 1.0
	v_pk_fma_f16 v128, v128, v128, -2.0 op_sel:[0,1,1] op_sel_hi:[1,1,0]
	v_cvt_scalef32_pk_fp8_f16 v137, v140, 1.0 op_sel:[0,0,1]
	v_cvt_scalef32_pk_fp8_f16 v138, v128, 1.0 op_sel:[0,0,1]
	v_mov_b32_e32 v140, v161
	v_mov_b32_e32 v141, v161
	v_mov_b32_e32 v142, v161
	v_mov_b32_e32 v143, v161
	v_mfma_scale_f32_32x32x64_f8f6f4 v[48:63], v[144:151], v[164:171], v[48:63], v227, v226 op_sel_hi:[0,0,0]
	v_mfma_scale_f32_32x32x64_f8f6f4 v[16:31], v[236:243], v[164:171], v[16:31], v227, v226 op_sel_hi:[0,0,0]
	ds_read_b128 v[128:131], v234 offset:40960
	ds_read_b128 v[132:135], v234 offset:41984
	s_waitcnt lgkmcnt(0)
	v_mfma_scale_f32_32x32x64_f8f6f4 v[96:111], v[128:135], v[156:163], v[96:111], v227, v226 op_sel_hi:[0,0,0]
	v_mfma_scale_f32_32x32x64_f8f6f4 v[112:127], v[128:135], v[136:143], v[112:127], v227, v226 op_sel_hi:[0,0,0]
	ds_read_b128 v[128:131], v234 offset:43008
	s_waitcnt lgkmcnt(0)
	v_mfma_scale_f32_32x32x64_f8f6f4 v[64:79], v[128:135], v[156:163], v[64:79], v227, v226 op_sel_hi:[0,0,0]
	v_mfma_scale_f32_32x32x64_f8f6f4 v[80:95], v[128:135], v[136:143], v[80:95], v227, v226 op_sel_hi:[0,0,0]
	ds_read_b128 v[128:131], v234 offset:45056
	s_waitcnt lgkmcnt(0)
	v_mfma_scale_f32_32x32x64_f8f6f4 v[32:47], v[128:135], v[156:163], v[32:47], v227, v226 op_sel_hi:[0,0,0]
	v_mfma_scale_f32_32x32x64_f8f6f4 v[48:63], v[128:135], v[136:143], v[48:63], v227, v226 op_sel_hi:[0,0,0]
	ds_read_b128 v[128:131], v234 offset:47104
	ds_read_b128 v[174:177], v234 offset:49152
	ds_read_b128 v[208:211], v234 offset:50176
	ds_read_b128 v[212:215], v234 offset:53248
	ds_read_b128 v[236:239], v234 offset:54272
	s_waitcnt lgkmcnt(4)
	v_mfma_scale_f32_32x32x64_f8f6f4 v[0:15], v[128:135], v[156:163], v[0:15], v227, v226 op_sel_hi:[0,0,0]
	v_mfma_scale_f32_32x32x64_f8f6f4 v[16:31], v[128:135], v[136:143], v[16:31], v227, v226 op_sel_hi:[0,0,0]
	s_nop 2
	v_cvt_pk_bf16_f32 v162, v96, v97 clamp
	v_cvt_pk_bf16_f32 v163, v98, v99 clamp
	v_cvt_pk_bf16_f32 v164, v100, v101 clamp
	v_cvt_pk_bf16_f32 v165, v102, v103 clamp
	v_cvt_pk_bf16_f32 v166, v112, v113 clamp
	v_cvt_pk_bf16_f32 v167, v114, v115 clamp
	v_cvt_pk_bf16_f32 v168, v116, v117 clamp
	v_cvt_pk_bf16_f32 v169, v118, v119 clamp
	v_cvt_pk_bf16_f32 v170, v104, v105 clamp
	v_cvt_pk_bf16_f32 v171, v106, v107 clamp
	v_cvt_pk_bf16_f32 v172, v108, v109 clamp
	v_add_u32_e32 v128, 0, v206
	v_cvt_pk_bf16_f32 v173, v110, v111 clamp
	v_add_u32_e32 v235, 0x18000, v128
	v_cvt_pk_bf16_f32 v202, v120, v121 clamp
	ds_read_b128 v[128:131], v235
	ds_read_b128 v[132:135], v235 offset:32
	ds_read_b128 v[136:139], v235 offset:64
	ds_read_b128 v[140:143], v235 offset:96
	v_cvt_pk_bf16_f32 v203, v122, v123 clamp
	ds_read_b128 v[96:99], v235 offset:128
	ds_read_b128 v[100:103], v235 offset:160
	ds_read_b128 v[104:107], v235 offset:192
	ds_read_b128 v[108:111], v235 offset:224
	v_cvt_pk_bf16_f32 v204, v124, v125 clamp
	v_cvt_pk_bf16_f32 v64, v64, v65
	s_waitcnt lgkmcnt(4)
	v_mfma_f32_32x32x16_bf16 v[144:159], v[174:177], v[166:169], v[128:143]
	v_cvt_pk_bf16_f32 v205, v126, v127 clamp
	ds_read_b128 v[240:243], v234 offset:57344
	ds_read_b128 v[244:247], v234 offset:58368
	ds_read_b128 v[248:251], v234 offset:61440
	ds_read_b128 v[252:255], v234 offset:62464
	v_cvt_pk_bf16_f32 v65, v74, v75 clamp
	v_cndmask_b32_e64 v230, v230, 0, s[14:15]
	v_mfma_f32_32x32x16_bf16 v[128:143], v[174:177], v[162:165], v[128:143]
	v_pk_max_i16 v174, v64, 0
	v_cvt_pk_bf16_f32 v175, v66, v67 clamp
	v_cvt_pk_bf16_f32 v176, v68, v69 clamp
	v_cvt_pk_bf16_f32 v177, v70, v71 clamp
	s_waitcnt lgkmcnt(4)
	v_mfma_f32_32x32x16_bf16 v[112:127], v[208:211], v[166:169], v[96:111]
	v_cvt_pk_bf16_f32 v80, v80, v81 clamp
	v_cvt_pk_bf16_f32 v81, v82, v83 clamp
	v_cvt_pk_bf16_f32 v82, v84, v85 clamp
	v_cvt_pk_bf16_f32 v83, v86, v87 clamp
	v_mfma_f32_32x32x16_bf16 v[96:111], v[208:211], v[162:165], v[96:111]
	v_cvt_pk_bf16_f32 v64, v72, v73 clamp
	v_cvt_pk_bf16_f32 v66, v76, v77 clamp
	v_cvt_pk_bf16_f32 v67, v78, v79 clamp
	v_cvt_pk_bf16_f32 v68, v88, v89 clamp
	v_cvt_pk_bf16_f32 v69, v90, v91 clamp
	v_cvt_pk_bf16_f32 v70, v92, v93 clamp
	v_cvt_pk_bf16_f32 v71, v94, v95 clamp
	v_add_u32_e32 v160, 0x14000, v234
	v_mfma_f32_32x32x16_bf16 v[128:143], v[212:215], v[170:173], v[128:143]
	v_mfma_f32_32x32x16_bf16 v[144:159], v[212:215], v[202:205], v[144:159]
	v_mfma_f32_32x32x16_bf16 v[96:111], v[236:239], v[170:173], v[96:111]
	v_mfma_f32_32x32x16_bf16 v[112:127], v[236:239], v[202:205], v[112:127]
	v_cvt_pk_bf16_f32 v76, v32, v33 clamp
	v_cvt_pk_bf16_f32 v77, v34, v35 clamp
	v_cvt_pk_bf16_f32 v78, v36, v37 clamp
	v_cvt_pk_bf16_f32 v79, v38, v39 clamp
	v_cvt_pk_bf16_f32 v88, v48, v49 clamp
	v_cvt_pk_bf16_f32 v89, v50, v51 clamp
	v_cvt_pk_bf16_f32 v90, v52, v53 clamp
	v_cvt_pk_bf16_f32 v91, v54, v55 clamp
	s_waitcnt lgkmcnt(3)
	v_mfma_f32_32x32x16_bf16 v[128:143], v[240:243], v[174:177], v[128:143]
	v_cvt_pk_bf16_f32 v72, v40, v41 clamp
	v_cvt_pk_bf16_f32 v73, v42, v43 clamp
	v_cvt_pk_bf16_f32 v74, v44, v45 clamp
	v_mfma_f32_32x32x16_bf16 v[144:159], v[240:243], v[80:83], v[144:159]
	ds_read_b128 v[92:95], v233 offset:16384
	ds_read_b128 v[208:211], v233 offset:17408
	ds_read_b128 v[236:239], v233 offset:20480
	ds_read_b128 v[240:243], v233 offset:21504
	v_cvt_pk_bf16_f32 v75, v46, v47 clamp
	v_cvt_pk_bf16_f32 v84, v56, v57 clamp
	v_cvt_pk_bf16_f32 v85, v58, v59 clamp
	s_waitcnt lgkmcnt(6)
	v_mfma_f32_32x32x16_bf16 v[96:111], v[244:247], v[174:177], v[96:111]
	v_cvt_pk_bf16_f32 v86, v60, v61 clamp
	v_cvt_pk_bf16_f32 v87, v62, v63 clamp
	v_mfma_f32_32x32x16_bf16 v[112:127], v[244:247], v[80:83], v[112:127]
	s_waitcnt lgkmcnt(5)
	v_mfma_f32_32x32x16_bf16 v[128:143], v[248:251], v[64:67], v[128:143]
	v_mfma_f32_32x32x16_bf16 v[144:159], v[248:251], v[68:71], v[144:159]
	s_waitcnt lgkmcnt(4)
	v_mfma_f32_32x32x16_bf16 v[96:111], v[252:255], v[64:67], v[96:111]
	v_mfma_f32_32x32x16_bf16 v[112:127], v[252:255], v[68:71], v[112:127]
	v_cvt_pk_bf16_f32 v206, v0, v1 clamp
	v_cvt_pk_bf16_f32 v207, v2, v3 clamp
	s_waitcnt lgkmcnt(2)
	v_mfma_f32_32x32x16_bf16 v[96:111], v[208:211], v[76:79], v[96:111]
	ds_read_b128 v[32:35], v233 offset:24576
	ds_read_b128 v[36:39], v233 offset:25600
	ds_read_b128 v[40:43], v233 offset:28672
	ds_read_b128 v[44:47], v233 offset:29696
	v_mfma_f32_32x32x16_bf16 v[112:127], v[208:211], v[88:91], v[112:127]
	v_cvt_pk_bf16_f32 v208, v4, v5 clamp
	v_cvt_pk_bf16_f32 v209, v6, v7 clamp
	v_cvt_pk_bf16_f32 v214, v16, v17 clamp
	v_cvt_pk_bf16_f32 v215, v18, v19 clamp
	v_cvt_pk_bf16_f32 v216, v20, v21 clamp
	v_cvt_pk_bf16_f32 v217, v22, v23 clamp
	v_mfma_f32_32x32x16_bf16 v[128:143], v[92:95], v[76:79], v[128:143]
	v_mfma_f32_32x32x16_bf16 v[144:159], v[92:95], v[88:91], v[144:159]
	v_cvt_pk_bf16_f32 v92, v8, v9 clamp
	v_cvt_pk_bf16_f32 v93, v10, v11 clamp
	v_cvt_pk_bf16_f32 v94, v12, v13 clamp
	v_cvt_pk_bf16_f32 v95, v14, v15 clamp
	v_cvt_pk_bf16_f32 v210, v24, v25 clamp
	v_cvt_pk_bf16_f32 v211, v26, v27 clamp
	v_cvt_pk_bf16_f32 v212, v28, v29 clamp
	v_cvt_pk_bf16_f32 v213, v30, v31 clamp
	s_waitcnt lgkmcnt(5)
	v_mfma_f32_32x32x16_bf16 v[128:143], v[236:239], v[72:75], v[128:143]
	v_mfma_f32_32x32x16_bf16 v[144:159], v[236:239], v[84:87], v[144:159]
	s_waitcnt lgkmcnt(4)
	v_mfma_f32_32x32x16_bf16 v[96:111], v[240:243], v[72:75], v[96:111]
	v_mfma_f32_32x32x16_bf16 v[112:127], v[240:243], v[84:87], v[112:127]
	s_waitcnt lgkmcnt(3)
	v_mfma_f32_32x32x16_bf16 v[128:143], v[32:35], v[206:209], v[128:143]
	ds_read_b128 v[0:3], v234 offset:51200
	ds_read_b128 v[236:239], v234 offset:52224
	ds_read_b128 v[240:243], v234 offset:55296
	ds_read_b128 v[244:247], v234 offset:56320
	v_mfma_f32_32x32x16_bf16 v[144:159], v[32:35], v[214:217], v[144:159]
	s_waitcnt lgkmcnt(6)
	v_mfma_f32_32x32x16_bf16 v[96:111], v[36:39], v[206:209], v[96:111]
	v_mfma_f32_32x32x16_bf16 v[112:127], v[36:39], v[214:217], v[112:127]
	s_waitcnt lgkmcnt(5)
	v_mfma_f32_32x32x16_bf16 v[128:143], v[40:43], v[92:95], v[128:143]
	v_mfma_f32_32x32x16_bf16 v[144:159], v[40:43], v[210:213], v[144:159]
	s_waitcnt lgkmcnt(4)
	v_mfma_f32_32x32x16_bf16 v[96:111], v[44:47], v[92:95], v[96:111]
	v_mfma_f32_32x32x16_bf16 v[112:127], v[44:47], v[210:213], v[112:127]
	ds_read_b128 v[32:35], v235 offset:256
	ds_read_b128 v[36:39], v235 offset:288
	ds_read_b128 v[40:43], v235 offset:320
	ds_read_b128 v[44:47], v235 offset:352
	s_nop 3
	v_cvt_pk_bf16_f32 v128, v128, v129 clamp
	v_cvt_pk_bf16_f32 v129, v130, v131 clamp
	v_cvt_pk_bf16_f32 v130, v132, v133 clamp
	v_cvt_pk_bf16_f32 v131, v134, v135 clamp
	s_waitcnt lgkmcnt(0)
	v_mfma_f32_32x32x16_bf16 v[48:63], v[0:3], v[166:169], v[32:47]
	v_cvt_pk_bf16_f32 v132, v144, v145 clamp
	v_cvt_pk_bf16_f32 v133, v146, v147 clamp
	v_cvt_pk_bf16_f32 v134, v148, v149 clamp
	v_cvt_pk_bf16_f32 v135, v150, v151 clamp
	v_mfma_f32_32x32x16_bf16 v[32:47], v[0:3], v[162:165], v[32:47]
	ds_read_b128 v[0:3], v235 offset:384
	ds_read_b128 v[4:7], v235 offset:416
	ds_read_b128 v[8:11], v235 offset:448
	ds_read_b128 v[12:15], v235 offset:480
	s_waitcnt lgkmcnt(0)
	v_mfma_f32_32x32x16_bf16 v[16:31], v[236:239], v[166:169], v[0:15]
	v_mfma_f32_32x32x16_bf16 v[0:15], v[236:239], v[162:165], v[0:15]
	ds_read_b128 v[162:165], v234 offset:59392
	ds_read_b128 v[166:169], v234 offset:60416
	ds_read_b128 v[236:239], v234 offset:63488
	ds_read_b128 v[248:251], v234 offset:64512
	v_mfma_f32_32x32x16_bf16 v[0:15], v[244:247], v[170:173], v[0:15]
	v_mfma_f32_32x32x16_bf16 v[32:47], v[240:243], v[170:173], v[32:47]
	v_mfma_f32_32x32x16_bf16 v[48:63], v[240:243], v[202:205], v[48:63]
	v_mfma_f32_32x32x16_bf16 v[16:31], v[244:247], v[202:205], v[16:31]
	s_waitcnt lgkmcnt(2)
	v_mfma_f32_32x32x16_bf16 v[0:15], v[166:169], v[174:177], v[0:15]
	v_cvt_pk_bf16_f32 v136, v136, v137 clamp
	v_cvt_pk_bf16_f32 v137, v138, v139 clamp
	v_cvt_pk_bf16_f32 v138, v140, v141 clamp
	v_cvt_pk_bf16_f32 v139, v142, v143 clamp
	v_cvt_pk_bf16_f32 v140, v152, v153 clamp
	v_mfma_f32_32x32x16_bf16 v[32:47], v[162:165], v[174:177], v[32:47]
	v_mfma_f32_32x32x16_bf16 v[48:63], v[162:165], v[80:83], v[48:63]
	v_mfma_f32_32x32x16_bf16 v[16:31], v[166:169], v[80:83], v[16:31]
	ds_read_b128 v[80:83], v233 offset:18432
	ds_read_b128 v[144:147], v233 offset:19456
	ds_read_b128 v[148:151], v233 offset:22528
	ds_read_b128 v[162:165], v233 offset:23552
	s_waitcnt lgkmcnt(4)
	v_mfma_f32_32x32x16_bf16 v[0:15], v[248:251], v[64:67], v[0:15]
	v_mfma_f32_32x32x16_bf16 v[32:47], v[236:239], v[64:67], v[32:47]
	v_cvt_pk_bf16_f32 v141, v154, v155 clamp
	v_cvt_pk_bf16_f32 v142, v156, v157 clamp
	v_cvt_pk_bf16_f32 v143, v158, v159 clamp
	v_mfma_f32_32x32x16_bf16 v[48:63], v[236:239], v[68:71], v[48:63]
	v_mfma_f32_32x32x16_bf16 v[16:31], v[248:251], v[68:71], v[16:31]
	s_waitcnt lgkmcnt(2)
	v_mfma_f32_32x32x16_bf16 v[0:15], v[144:147], v[76:79], v[0:15]
	v_mfma_f32_32x32x16_bf16 v[32:47], v[80:83], v[76:79], v[32:47]
	v_mfma_f32_32x32x16_bf16 v[48:63], v[80:83], v[88:91], v[48:63]
	ds_read_b128 v[64:67], v233 offset:26624
	ds_read_b128 v[68:71], v233 offset:27648
	ds_read_b128 v[76:79], v233 offset:30720
	ds_read_b128 v[80:83], v233 offset:31744
	v_mfma_f32_32x32x16_bf16 v[16:31], v[144:147], v[88:91], v[16:31]
	v_cvt_pk_bf16_f32 v96, v96, v97 clamp
	v_cvt_pk_bf16_f32 v97, v98, v99 clamp
	v_cvt_pk_bf16_f32 v98, v100, v101 clamp
	v_cvt_pk_bf16_f32 v99, v102, v103 clamp
	s_waitcnt lgkmcnt(4)
	v_mfma_f32_32x32x16_bf16 v[0:15], v[162:165], v[72:75], v[0:15]
	v_cvt_pk_bf16_f32 v100, v112, v113 clamp
	v_mfma_f32_32x32x16_bf16 v[32:47], v[148:151], v[72:75], v[32:47]
	v_cvt_pk_bf16_f32 v101, v114, v115 clamp
	v_cvt_pk_bf16_f32 v102, v116, v117 clamp
	v_cvt_pk_bf16_f32 v103, v118, v119 clamp
	v_mfma_f32_32x32x16_bf16 v[48:63], v[148:151], v[84:87], v[48:63]
	v_mfma_f32_32x32x16_bf16 v[16:31], v[162:165], v[84:87], v[16:31]
	s_waitcnt lgkmcnt(2)
	v_mfma_f32_32x32x16_bf16 v[0:15], v[68:71], v[206:209], v[0:15]
	ds_read_b128 v[84:87], v160
	ds_read_b128 v[112:115], v160 offset:1024
	ds_read_b128 v[116:119], v160 offset:2048
	ds_read_b128 v[144:147], v160 offset:3072
	v_mfma_f32_32x32x16_bf16 v[32:47], v[64:67], v[206:209], v[32:47]
	v_mfma_f32_32x32x16_bf16 v[48:63], v[64:67], v[214:217], v[48:63]
	v_cvt_pk_bf16_f32 v104, v104, v105 clamp
	v_cvt_pk_bf16_f32 v105, v106, v107 clamp
	v_cvt_pk_bf16_f32 v106, v108, v109 clamp
	v_cvt_pk_bf16_f32 v107, v110, v111 clamp
	v_mfma_f32_32x32x16_bf16 v[16:31], v[68:71], v[214:217], v[16:31]
	v_cvt_pk_bf16_f32 v108, v120, v121 clamp
	v_cvt_pk_bf16_f32 v109, v122, v123 clamp
	v_cvt_pk_bf16_f32 v110, v124, v125 clamp
	s_waitcnt lgkmcnt(4)
	v_mfma_f32_32x32x16_bf16 v[0:15], v[80:83], v[92:95], v[0:15]
	v_cvt_pk_bf16_f32 v111, v126, v127 clamp
	v_mfma_f32_32x32x16_bf16 v[32:47], v[76:79], v[92:95], v[32:47]
	v_mfma_f32_32x32x16_bf16 v[48:63], v[76:79], v[210:213], v[48:63]
	v_mfma_f32_32x32x16_bf16 v[16:31], v[80:83], v[210:213], v[16:31]
	s_waitcnt lgkmcnt(3)
	v_mfma_f32_4x4x4_16b_bf16 v[64:67], v[84:85], v[128:129], 0
	v_mfma_f32_4x4x4_16b_bf16 v[68:71], v[86:87], v[130:131], 0
	s_nop 7
	v_cvt_pk_bf16_f32 v32, v32, v33 clamp
	v_cvt_pk_bf16_f32 v33, v34, v35 clamp
	v_cvt_pk_bf16_f32 v34, v36, v37 clamp
	v_cvt_pk_bf16_f32 v35, v38, v39 clamp
	v_mfma_f32_4x4x4_16b_bf16 v[80:83], v[84:85], v[132:133], 0
	v_mfma_f32_4x4x4_16b_bf16 v[88:91], v[86:87], v[134:135], 0
	v_cvt_pk_bf16_f32 v48, v48, v49 clamp
	v_cvt_pk_bf16_f32 v49, v50, v51 clamp
	v_cvt_pk_bf16_f32 v50, v52, v53 clamp
	v_cvt_pk_bf16_f32 v51, v54, v55 clamp
	s_waitcnt lgkmcnt(2)
	v_mfma_f32_4x4x4_16b_bf16 v[64:67], v[112:113], v[136:137], v[64:67]
	v_mfma_f32_4x4x4_16b_bf16 v[68:71], v[114:115], v[138:139], v[68:71]
	v_cvt_pk_bf16_f32 v40, v40, v41 clamp
	v_cvt_pk_bf16_f32 v41, v42, v43 clamp
	v_cvt_pk_bf16_f32 v42, v44, v45 clamp
	v_cvt_pk_bf16_f32 v43, v46, v47 clamp
	v_mfma_f32_4x4x4_16b_bf16 v[80:83], v[112:113], v[140:141], v[80:83]
	v_mfma_f32_4x4x4_16b_bf16 v[88:91], v[114:115], v[142:143], v[88:91]
	s_waitcnt lgkmcnt(1)
	v_mfma_f32_4x4x4_16b_bf16 v[64:67], v[116:117], v[96:97], v[64:67]
	v_mfma_f32_4x4x4_16b_bf16 v[68:71], v[118:119], v[98:99], v[68:71]
	ds_read_b128 v[36:39], v160 offset:4096
	ds_read_b128 v[96:99], v160 offset:5120
	v_cvt_pk_bf16_f32 v0, v0, v1 clamp
	v_cvt_pk_bf16_f32 v1, v2, v3 clamp
	v_cvt_pk_bf16_f32 v2, v4, v5 clamp
	v_cvt_pk_bf16_f32 v3, v6, v7 clamp
	v_mfma_f32_4x4x4_16b_bf16 v[80:83], v[116:117], v[100:101], v[80:83]
	v_mfma_f32_4x4x4_16b_bf16 v[88:91], v[118:119], v[102:103], v[88:91]
	ds_read_b128 v[4:7], v160 offset:7168
	v_cvt_pk_bf16_f32 v12, v12, v13
	v_cvt_pk_bf16_f32 v24, v24, v25
	v_cvt_pk_bf16_f32 v25, v26, v27
	s_waitcnt lgkmcnt(3)
	v_mfma_f32_4x4x4_16b_bf16 v[64:67], v[144:145], v[104:105], v[64:67]
	v_mfma_f32_4x4x4_16b_bf16 v[68:71], v[146:147], v[106:107], v[68:71]
	v_cndmask_b32_e64 v219, v219, 0, s[14:15]
	v_cndmask_b32_e64 v218, v218, 0, s[14:15]
	v_mfma_f32_4x4x4_16b_bf16 v[80:83], v[144:145], v[108:109], v[80:83]
	v_mfma_f32_4x4x4_16b_bf16 v[88:91], v[146:147], v[110:111], v[88:91]
	s_waitcnt lgkmcnt(2)
	v_mfma_f32_4x4x4_16b_bf16 v[64:67], v[36:37], v[32:33], v[64:67]
	v_mfma_f32_4x4x4_16b_bf16 v[68:71], v[38:39], v[34:35], v[68:71]
	v_cvt_pk_bf16_f32 v34, v20, v21
	v_cvt_pk_bf16_f32 v35, v22, v23
	ds_read_b128 v[20:23], v160 offset:6144
	v_cvt_pk_bf16_f32 v32, v16, v17
	v_cvt_pk_bf16_f32 v33, v18, v19
	v_cvt_pk_bf16_f32 v16, v56, v57 clamp
	v_cvt_pk_bf16_f32 v17, v58, v59 clamp
	v_mfma_f32_4x4x4_16b_bf16 v[80:83], v[36:37], v[48:49], v[80:83]
	v_mfma_f32_4x4x4_16b_bf16 v[88:91], v[38:39], v[50:51], v[88:91]
	v_cvt_pk_bf16_f32 v18, v60, v61 clamp
	v_cvt_pk_bf16_f32 v19, v62, v63 clamp
	s_waitcnt lgkmcnt(2)
	v_mfma_f32_4x4x4_16b_bf16 v[64:67], v[96:97], v[40:41], v[64:67]
	v_mfma_f32_4x4x4_16b_bf16 v[68:71], v[98:99], v[42:43], v[68:71]
	v_mfma_f32_4x4x4_16b_bf16 v[80:83], v[96:97], v[16:17], v[80:83]
	v_mfma_f32_4x4x4_16b_bf16 v[88:91], v[98:99], v[18:19], v[88:91]
	v_cvt_pk_bf16_f32 v16, v8, v9
	v_cvt_pk_bf16_f32 v17, v10, v11
	v_pk_max_i16 v8, v24, 0
	v_pk_max_i16 v9, v25, 0
	v_cvt_pk_bf16_f32 v10, v28, v29 clamp
	v_cvt_pk_bf16_f32 v11, v30, v31 clamp
	s_waitcnt lgkmcnt(0)
	v_mfma_f32_4x4x4_16b_bf16 v[64:67], v[20:21], v[0:1], v[64:67]
	v_mfma_f32_4x4x4_16b_bf16 v[68:71], v[22:23], v[2:3], v[68:71]
	v_pk_max_i16 v0, v32, 0
	v_pk_max_i16 v1, v33, 0
	v_pk_max_i16 v2, v34, 0
	v_pk_max_i16 v3, v35, 0
	s_nop 1
	v_mfma_f32_4x4x4_16b_bf16 v[80:83], v[20:21], v[0:1], v[80:83]
	v_mfma_f32_4x4x4_16b_bf16 v[88:91], v[22:23], v[2:3], v[88:91]
	v_pk_max_i16 v0, v16, 0
	v_pk_max_i16 v1, v17, 0
	v_pk_max_i16 v2, v12, 0
	v_cvt_pk_bf16_f32 v3, v14, v15 clamp
	s_nop 1
	v_mfma_f32_4x4x4_16b_bf16 v[64:67], v[4:5], v[0:1], v[64:67]
	v_mfma_f32_4x4x4_16b_bf16 v[68:71], v[6:7], v[2:3], v[68:71]
	v_mfma_f32_4x4x4_16b_bf16 v[80:83], v[4:5], v[8:9], v[80:83]
	v_mfma_f32_4x4x4_16b_bf16 v[88:91], v[6:7], v[10:11], v[88:91]
	s_waitcnt vmcnt(10)
	s_nop 3
	v_pk_add_f32 v[64:65], v[64:65], v[68:69]
	v_pk_add_f32 v[80:81], v[80:81], v[88:89]
	v_add_f32_e32 v66, v66, v70
	v_add_f32_e32 v82, v82, v90
	s_nop 1
	v_permlane32_swap_b32_e32 v64, v80
	v_permlane32_swap_b32_e32 v65, v81
	v_permlane32_swap_b32_e32 v66, v82
	s_nop 0
	v_add_f32_e32 v64, v64, v80
	v_add_f32_e32 v65, v65, v81
	v_add_f32_e32 v66, v66, v82
	v_add_f32_e32 v3, s10, v64
	v_add_f32_e32 v4, s11, v65
	v_add_f32_e32 v5, s18, v66
	v_mul_f32_e32 v3, 0xbfb8aa3b, v3
	v_mul_f32_e32 v4, 0xbfb8aa3b, v4
	v_mul_f32_e32 v5, 0xbfb8aa3b, v5
	v_exp_f32_e32 v3, v3
	v_exp_f32_e32 v4, v4
	v_exp_f32_e32 v5, v5
	v_add_f32_e32 v3, 1.0, v3
	v_add_f32_e32 v4, 1.0, v4
	v_add_f32_e32 v5, 1.0, v5
	v_rcp_f32_e32 v3, v3
	v_rcp_f32_e32 v4, v4
	v_rcp_f32_e32 v5, v5
	v_fmac_f32_e32 v218, v232, v3
	v_fmac_f32_e32 v219, v232, v4
	v_fmac_f32_e32 v230, v232, v5
	s_andn2_b64 vcc, exec, s[12:13]
	s_cbranch_vccnz .LBB1_6
	v_add_f32_dpp v218, v218, v218 row_shr:1 row_mask:0xf bank_mask:0xf bound_ctrl:1
	v_add_f32_dpp v219, v219, v219 row_shr:1 row_mask:0xf bank_mask:0xf bound_ctrl:1
	v_add_f32_dpp v230, v230, v230 row_shr:1 row_mask:0xf bank_mask:0xf bound_ctrl:1
	v_add_f32_dpp v218, v218, v218 row_shr:2 row_mask:0xf bank_mask:0xf bound_ctrl:1
	v_add_f32_dpp v219, v219, v219 row_shr:2 row_mask:0xf bank_mask:0xf bound_ctrl:1
	v_add_f32_dpp v230, v230, v230 row_shr:2 row_mask:0xf bank_mask:0xf bound_ctrl:1
	v_add_f32_dpp v218, v218, v218 row_shr:4 row_mask:0xf bank_mask:0xf bound_ctrl:1
	v_add_f32_dpp v219, v219, v219 row_shr:4 row_mask:0xf bank_mask:0xf bound_ctrl:1
	v_add_f32_dpp v230, v230, v230 row_shr:4 row_mask:0xf bank_mask:0xf bound_ctrl:1
	v_add_f32_dpp v218, v218, v218 row_shr:8 row_mask:0xf bank_mask:0xf bound_ctrl:1
	v_add_f32_dpp v219, v219, v219 row_shr:8 row_mask:0xf bank_mask:0xf bound_ctrl:1
	v_add_f32_dpp v230, v230, v230 row_shr:8 row_mask:0xf bank_mask:0xf bound_ctrl:1
	v_mov_b32_e32 v0, 0
	v_mov_b32_e32 v1, 0
	v_mov_b32_e32 v5, 0
	v_mov_b32_dpp v0, v218 row_bcast:15 row_mask:0xa bank_mask:0xf
	v_mov_b32_dpp v1, v219 row_bcast:15 row_mask:0xa bank_mask:0xf
	v_mov_b32_dpp v5, v230 row_bcast:15 row_mask:0xa bank_mask:0xf
	v_lshl_add_u32 v6, v231, 1, v231
	v_ashrrev_i32_e32 v7, 31, v6
	v_add_f32_e32 v218, v218, v0
	v_add_f32_e32 v219, v219, v1
	v_add_f32_e32 v230, v230, v5
	v_mov_b32_e32 v0, 0
	v_mov_b32_e32 v1, 0
	v_mov_b32_e32 v5, 0
	v_mov_b32_dpp v0, v218 row_bcast:31 row_mask:0xc bank_mask:0xf
	v_mov_b32_dpp v1, v219 row_bcast:31 row_mask:0xc bank_mask:0xf
	v_mov_b32_dpp v5, v230 row_bcast:31 row_mask:0xc bank_mask:0xf
	v_lshl_add_u64 v[6:7], v[6:7], 2, s[8:9]
	v_cmp_eq_u32_e32 vcc, 63, v220
	v_add_f32_e32 v2, v218, v0
	v_add_f32_e32 v3, v219, v1
	v_add_f32_e32 v4, v230, v5
	s_and_saveexec_b64 s[12:13], vcc
	global_store_dwordx3 v[6:7], v[2:4], off
	s_branch .LBB1_5
